# v53 + P6 unit header: removed the vmcnt(1)/vmcnt(0) drain that only waited for the previous unit's scatter stores
# baseline (speedup 1.0000x reference)
;     ...
;         for (int t = 0; t < nt - 2; t += 2) {
;             G_TILE(G_A0, G_B0, true, G_B1, G_A1, t + 1, true, t + 2, (void)0);
.LBB0_861:
	s_andn2_b64 vcc, exec, s[28:29]
	v_mov_b32_e32 v175, 0
	s_cbranch_vccnz .LBB0_864
	s_mov_b32 s8, 0
	s_mov_b32 s9, 0x1e0000
	s_movk_i32 s36, 0x100
	s_cmp_lt_u32 s99, 9
	s_cbranch_scc1 .Lslow_P6
	s_mov_b32 m0, s85
	s_add_i32 s38, s36, 0xffffff80
	ds_read_b64_tr_b16 v[178:179], v206
	ds_read_b64_tr_b16 v[176:177], v205
	ds_read_b64_tr_b16 v[180:181], v205 offset:32
	ds_read_b64_tr_b16 v[184:185], v205 offset:64
	ds_read_b64_tr_b16 v[188:189], v205 offset:96
	ds_read_b128 v[192:195], v199
	ds_read_b64_tr_b16 v[182:183], v206 offset:32
	ds_read_b64_tr_b16 v[186:187], v206 offset:64
	ds_read_b64_tr_b16 v[190:191], v206 offset:96
	ds_read_b128 v[208:211], v199 offset:2048
	ds_read_b128 v[212:215], v199 offset:4096
	buffer_load_dwordx4 v200, s[20:23], s38 offen lds
	s_mov_b32 m0, s86
	s_waitcnt lgkmcnt(0)
	v_mfma_f32_16x16x32_bf16 v[172:175], v[176:179], v[192:195], 0
	buffer_load_dwordx4 v201, s[20:23], s38 offen lds
	v_mfma_f32_16x16x32_bf16 v[168:171], v[180:183], v[192:195], 0
	v_mfma_f32_16x16x32_bf16 v[164:167], v[184:187], v[192:195], 0
	v_mfma_f32_16x16x32_bf16 v[160:163], v[188:191], v[192:195], 0
	v_mfma_f32_16x16x32_bf16 v[156:159], v[176:179], v[208:211], 0
	s_mov_b32 m0, s87
	s_nop 0
	buffer_load_dwordx4 v202, s[20:23], s38 offen lds
	ds_read_b128 v[192:195], v199 offset:6144
	s_waitcnt vmcnt(10)
	v_cvt_pk_bf16_f32 v23, v22, v23
	v_cvt_pk_bf16_f32 v22, v20, v21
	v_mfma_f32_16x16x32_bf16 v[152:155], v[180:183], v[208:211], 0
	ds_write_b64 v198, v[22:23] offset:34816
	v_mfma_f32_16x16x32_bf16 v[148:151], v[184:187], v[208:211], 0
	s_mov_b32 m0, s88
	s_nop 0
	buffer_load_dwordx4 v203, s[20:23], s38 offen lds
	v_mfma_f32_16x16x32_bf16 v[144:147], v[188:191], v[208:211], 0
	v_mfma_f32_16x16x32_bf16 v[132:135], v[176:179], v[212:215], 0
	s_mov_b32 m0, s89
	s_nop 0
	buffer_load_dwordx4 v204, s[20:23], s38 offen lds
	s_add_i32 s38, s9, 0xfff20000
	ds_read_b128 v[208:211], v199 offset:8192
	v_mfma_f32_16x16x32_bf16 v[124:127], v[180:183], v[212:215], 0
	v_mfma_f32_16x16x32_bf16 v[120:123], v[184:187], v[212:215], 0
	v_mfma_f32_16x16x32_bf16 v[140:143], v[188:191], v[212:215], 0
	s_waitcnt lgkmcnt(2)
	v_mfma_f32_16x16x32_bf16 v[136:139], v[176:179], v[192:195], 0
	ds_read_b128 v[212:215], v199 offset:10240
	buffer_load_dwordx4 v[20:23], v197, s[24:27], s38 offen
	s_waitcnt vmcnt(11)
	v_cvt_pk_bf16_f32 v31, v30, v31
	v_cvt_pk_bf16_f32 v30, v28, v29
	v_mfma_f32_16x16x32_bf16 v[128:131], v[180:183], v[192:195], 0
	ds_write_b64 v198, v[30:31] offset:43520
	v_mfma_f32_16x16x32_bf16 v[116:119], v[184:187], v[192:195], 0
	v_mfma_f32_16x16x32_bf16 v[112:115], v[188:191], v[192:195], 0
	s_add_i32 s39, s9, 0xfff40000
	s_waitcnt lgkmcnt(2)
	v_mfma_f32_16x16x32_bf16 v[100:103], v[176:179], v[208:211], 0
	ds_read_b128 v[192:195], v199 offset:12288
	v_mfma_f32_16x16x32_bf16 v[92:95], v[180:183], v[208:211], 0
	v_mfma_f32_16x16x32_bf16 v[88:91], v[184:187], v[208:211], 0
	v_mfma_f32_16x16x32_bf16 v[108:111], v[188:191], v[208:211], 0
	s_waitcnt lgkmcnt(2)
	v_mfma_f32_16x16x32_bf16 v[104:107], v[176:179], v[212:215], 0
	ds_read_b128 v[208:211], v199 offset:14336
	v_cvt_pk_bf16_f32 v19, v18, v19
	v_cvt_pk_bf16_f32 v18, v16, v17
	v_mfma_f32_16x16x32_bf16 v[96:99], v[180:183], v[212:215], 0
	ds_write_b64 v198, v[18:19] offset:52224
	v_mfma_f32_16x16x32_bf16 v[84:87], v[184:187], v[212:215], 0
	v_mfma_f32_16x16x32_bf16 v[80:83], v[188:191], v[212:215], 0
	s_add_i32 s43, s9, 0xfff60000
	buffer_load_dwordx4 v[28:31], v197, s[24:27], s39 offen
	s_waitcnt lgkmcnt(2)
	v_mfma_f32_16x16x32_bf16 v[72:75], v[176:179], v[192:195], 0
	ds_read_b128 v[212:215], v199 offset:16384
	v_mfma_f32_16x16x32_bf16 v[64:67], v[180:183], v[192:195], 0
	v_mfma_f32_16x16x32_bf16 v[60:63], v[184:187], v[192:195], 0
	v_mfma_f32_16x16x32_bf16 v[76:79], v[188:191], v[192:195], 0
	s_waitcnt lgkmcnt(2)
	v_mfma_f32_16x16x32_bf16 v[68:71], v[176:179], v[208:211], 0
	ds_read_b128 v[192:195], v199 offset:1024
	buffer_load_dwordx4 v[16:19], v197, s[24:27], s43 offen
	s_waitcnt vmcnt(12)
	v_cvt_pk_bf16_f32 v27, v26, v27
	v_cvt_pk_bf16_f32 v26, v24, v25
	v_mfma_f32_16x16x32_bf16 v[56:59], v[180:183], v[208:211], 0
	ds_write_b64 v198, v[26:27] offset:60928
	v_mfma_f32_16x16x32_bf16 v[52:55], v[184:187], v[208:211], 0
	v_mfma_f32_16x16x32_bf16 v[48:51], v[188:191], v[208:211], 0
	s_add_i32 s45, s9, 0xfff80000
	ds_read_b128 v[208:211], v199 offset:3072
	s_waitcnt lgkmcnt(3)
	v_mfma_f32_16x16x32_bf16 v[44:47], v[176:179], v[212:215], 0
	ds_read_b64_tr_b16 v[246:247], v206 offset:17408
	ds_read_b64_tr_b16 v[218:219], v206 offset:17440
	ds_read_b64_tr_b16 v[244:245], v205 offset:17408
	ds_read_b64_tr_b16 v[216:217], v205 offset:17440
	v_mfma_f32_16x16x32_bf16 v[40:43], v[180:183], v[212:215], 0
	ds_read_b64_tr_b16 v[248:249], v205 offset:17472
	ds_read_b64_tr_b16 v[250:251], v206 offset:17472
	v_mfma_f32_16x16x32_bf16 v[36:39], v[184:187], v[212:215], 0
	ds_read_b64_tr_b16 v[252:253], v205 offset:17504
	ds_read_b64_tr_b16 v[254:255], v206 offset:17504
	v_mfma_f32_16x16x32_bf16 v[32:35], v[188:191], v[212:215], 0
	s_waitcnt lgkmcnt(5)
	v_mfma_f32_16x16x32_bf16 v[172:175], v[244:247], v[192:195], v[172:175]
	ds_read_b128 v[188:191], v199 offset:5120
	buffer_load_dwordx4 v[24:27], v197, s[24:27], s45 offen
	s_waitcnt vmcnt(12)
	v_cvt_pk_bf16_f32 v15, v14, v15
	v_cvt_pk_bf16_f32 v14, v12, v13
	s_waitcnt lgkmcnt(5)
	v_mfma_f32_16x16x32_bf16 v[168:171], v[216:219], v[192:195], v[168:171]
	ds_write_b64 v198, v[14:15] offset:35072
	s_waitcnt lgkmcnt(4)
	v_mfma_f32_16x16x32_bf16 v[164:167], v[248:251], v[192:195], v[164:167]
	s_waitcnt lgkmcnt(2)
; #define G_ENDTILE(VM) do { asm volatile("s_waitcnt vmcnt(" #VM ")" ::: "memory"); \
;         asm volatile("s_waitcnt lgkmcnt(0)" ::: "memory"); __builtin_amdgcn_s_barrier(); asm volatile("" ::: "memory"); } while (0)
;     ...
;             G_TILE(G_A0, G_B0, true, G_B1, G_A1, t + 1, true, t + 2, (void)0);
;             G_ENDTILE(8);
;             G_TILE(G_A1, G_B1, true, G_B0, G_A0, t + 2, true, t + 3, (void)0);
	v_mfma_f32_16x16x32_bf16 v[160:163], v[252:255], v[192:195], v[160:163]
	v_mfma_f32_16x16x32_bf16 v[156:159], v[244:247], v[208:211], v[156:159]
	ds_read_b128 v[192:195], v199 offset:7168
	v_mfma_f32_16x16x32_bf16 v[152:155], v[216:219], v[208:211], v[152:155]
	v_mfma_f32_16x16x32_bf16 v[148:151], v[248:251], v[208:211], v[148:151]
	v_mfma_f32_16x16x32_bf16 v[144:147], v[252:255], v[208:211], v[144:147]
	s_waitcnt lgkmcnt(2)
	v_mfma_f32_16x16x32_bf16 v[132:135], v[244:247], v[188:191], v[132:135]
	ds_read_b128 v[208:211], v199 offset:9216
	buffer_load_dwordx4 v[12:15], v197, s[16:19], s38 offen
	s_waitcnt vmcnt(11)
	v_cvt_pk_bf16_f32 v7, v6, v7
	v_cvt_pk_bf16_f32 v6, v4, v5
	v_mfma_f32_16x16x32_bf16 v[124:127], v[216:219], v[188:191], v[124:127]
	ds_write_b64 v198, v[6:7] offset:43776
	v_mfma_f32_16x16x32_bf16 v[120:123], v[248:251], v[188:191], v[120:123]
	v_mfma_f32_16x16x32_bf16 v[140:143], v[252:255], v[188:191], v[140:143]
	s_waitcnt lgkmcnt(2)
	v_mfma_f32_16x16x32_bf16 v[136:139], v[244:247], v[192:195], v[136:139]
	ds_read_b128 v[188:191], v199 offset:11264
	v_mfma_f32_16x16x32_bf16 v[128:131], v[216:219], v[192:195], v[128:131]
	v_mfma_f32_16x16x32_bf16 v[116:119], v[248:251], v[192:195], v[116:119]
	v_mfma_f32_16x16x32_bf16 v[112:115], v[252:255], v[192:195], v[112:115]
	s_waitcnt lgkmcnt(2)
	v_mfma_f32_16x16x32_bf16 v[100:103], v[244:247], v[208:211], v[100:103]
	ds_read_b128 v[192:195], v199 offset:13312
	v_cvt_pk_bf16_f32 v3, v2, v3
	v_cvt_pk_bf16_f32 v2, v0, v1
	v_mfma_f32_16x16x32_bf16 v[92:95], v[216:219], v[208:211], v[92:95]
	ds_write_b64 v198, v[2:3] offset:52480
	v_mfma_f32_16x16x32_bf16 v[88:91], v[248:251], v[208:211], v[88:91]
	v_mfma_f32_16x16x32_bf16 v[108:111], v[252:255], v[208:211], v[108:111]
	buffer_load_dwordx4 v[4:7], v197, s[16:19], s39 offen
	s_waitcnt lgkmcnt(2)
	v_mfma_f32_16x16x32_bf16 v[104:107], v[244:247], v[188:191], v[104:107]
	ds_read_b128 v[208:211], v199 offset:15360
	v_mfma_f32_16x16x32_bf16 v[96:99], v[216:219], v[188:191], v[96:99]
	v_mfma_f32_16x16x32_bf16 v[84:87], v[248:251], v[188:191], v[84:87]
	v_mfma_f32_16x16x32_bf16 v[80:83], v[252:255], v[188:191], v[80:83]
	s_waitcnt lgkmcnt(2)
	v_mfma_f32_16x16x32_bf16 v[72:75], v[244:247], v[192:195], v[72:75]
	ds_read_b128 v[236:239], v199 offset:17408
	buffer_load_dwordx4 v[0:3], v197, s[16:19], s43 offen
	s_waitcnt vmcnt(12)
	v_cvt_pk_bf16_f32 v11, v10, v11
	v_cvt_pk_bf16_f32 v10, v8, v9
	v_mfma_f32_16x16x32_bf16 v[64:67], v[216:219], v[192:195], v[64:67]
	ds_write_b64 v198, v[10:11] offset:61184
	v_mfma_f32_16x16x32_bf16 v[60:63], v[248:251], v[192:195], v[60:63]
	v_mfma_f32_16x16x32_bf16 v[76:79], v[252:255], v[192:195], v[76:79]
	s_waitcnt lgkmcnt(2)
	v_mfma_f32_16x16x32_bf16 v[68:71], v[244:247], v[208:211], v[68:71]
	v_mfma_f32_16x16x32_bf16 v[56:59], v[216:219], v[208:211], v[56:59]
	v_mfma_f32_16x16x32_bf16 v[52:55], v[248:251], v[208:211], v[52:55]
	v_mfma_f32_16x16x32_bf16 v[48:51], v[252:255], v[208:211], v[48:51]
	s_waitcnt lgkmcnt(1)
	buffer_load_dwordx4 v[8:11], v197, s[16:19], s45 offen
	s_waitcnt vmcnt(8)
	s_mov_b32 m0, s49
	s_waitcnt lgkmcnt(0)
	s_barrier
	ds_read_b64_tr_b16 v[178:179], v206 offset:34816
	ds_read_b64_tr_b16 v[176:177], v205 offset:34816
	ds_read_b64_tr_b16 v[180:181], v205 offset:34848
	ds_read_b64_tr_b16 v[184:185], v205 offset:34880
	ds_read_b64_tr_b16 v[188:189], v205 offset:34912
	ds_read_b128 v[192:195], v199 offset:36864
	ds_read_b64_tr_b16 v[182:183], v206 offset:34848
	ds_read_b64_tr_b16 v[186:187], v206 offset:34880
	ds_read_b64_tr_b16 v[190:191], v206 offset:34912
	ds_read_b128 v[208:211], v199 offset:38912
	ds_read_b128 v[212:215], v199 offset:40960
	buffer_load_dwordx4 v200, s[20:23], s36 offen lds
	s_mov_b32 m0, s68
	v_mfma_f32_16x16x32_bf16 v[44:47], v[244:247], v[236:239], v[44:47]
	v_mfma_f32_16x16x32_bf16 v[40:43], v[216:219], v[236:239], v[40:43]
	v_mfma_f32_16x16x32_bf16 v[36:39], v[248:251], v[236:239], v[36:39]
	v_mfma_f32_16x16x32_bf16 v[32:35], v[252:255], v[236:239], v[32:35]
	s_waitcnt lgkmcnt(5)
	v_mfma_f32_16x16x32_bf16 v[172:175], v[176:179], v[192:195], v[172:175]
	buffer_load_dwordx4 v201, s[20:23], s36 offen lds
	s_add_i32 s38, s9, 0xfffa0000
	s_waitcnt lgkmcnt(4)
	v_mfma_f32_16x16x32_bf16 v[168:171], v[180:183], v[192:195], v[168:171]
	s_waitcnt lgkmcnt(3)
	v_mfma_f32_16x16x32_bf16 v[164:167], v[184:187], v[192:195], v[164:167]
	s_waitcnt lgkmcnt(2)
	v_mfma_f32_16x16x32_bf16 v[160:163], v[188:191], v[192:195], v[160:163]
	s_waitcnt lgkmcnt(1)
	v_mfma_f32_16x16x32_bf16 v[156:159], v[176:179], v[208:211], v[156:159]
	s_mov_b32 m0, s77
	s_nop 0
	buffer_load_dwordx4 v202, s[20:23], s36 offen lds
	ds_read_b128 v[192:195], v199 offset:43008
	s_waitcnt vmcnt(10)
	v_cvt_pk_bf16_f32 v23, v22, v23
	v_cvt_pk_bf16_f32 v22, v20, v21
	v_mfma_f32_16x16x32_bf16 v[152:155], v[180:183], v[208:211], v[152:155]
	ds_write_b64 v198, v[22:23]
	v_mfma_f32_16x16x32_bf16 v[148:151], v[184:187], v[208:211], v[148:151]
	s_mov_b32 m0, s78
	s_nop 0
	buffer_load_dwordx4 v203, s[20:23], s36 offen lds
	v_mfma_f32_16x16x32_bf16 v[144:147], v[188:191], v[208:211], v[144:147]
	s_waitcnt lgkmcnt(2)
	v_mfma_f32_16x16x32_bf16 v[132:135], v[176:179], v[212:215], v[132:135]
	s_mov_b32 m0, s79
	s_nop 0
	buffer_load_dwordx4 v204, s[20:23], s36 offen lds
	ds_read_b128 v[208:211], v199 offset:45056
	v_mfma_f32_16x16x32_bf16 v[124:127], v[180:183], v[212:215], v[124:127]
	v_mfma_f32_16x16x32_bf16 v[120:123], v[184:187], v[212:215], v[120:123]
	v_mfma_f32_16x16x32_bf16 v[140:143], v[188:191], v[212:215], v[140:143]
	s_waitcnt lgkmcnt(2)
; #define G_ENDTILE(VM) do { asm volatile("s_waitcnt vmcnt(" #VM ")" ::: "memory"); \
;         asm volatile("s_waitcnt lgkmcnt(0)" ::: "memory"); __builtin_amdgcn_s_barrier(); asm volatile("" ::: "memory"); } while (0)
;     ...
;             G_TILE(G_A1, G_B1, true, G_B0, G_A0, t + 2, true, t + 3, (void)0);
;             G_ENDTILE(8);
	v_mfma_f32_16x16x32_bf16 v[136:139], v[176:179], v[192:195], v[136:139]
	ds_read_b128 v[212:215], v199 offset:47104
	buffer_load_dwordx4 v[20:23], v197, s[24:27], s38 offen
	s_waitcnt vmcnt(12)
	v_cvt_pk_bf16_f32 v31, v30, v31
	v_cvt_pk_bf16_f32 v30, v28, v29
	v_mfma_f32_16x16x32_bf16 v[128:131], v[180:183], v[192:195], v[128:131]
	ds_write_b64 v198, v[30:31] offset:8704
	v_mfma_f32_16x16x32_bf16 v[116:119], v[184:187], v[192:195], v[116:119]
	v_mfma_f32_16x16x32_bf16 v[112:115], v[188:191], v[192:195], v[112:115]
	s_add_i32 s39, s9, 0xfffc0000
	s_waitcnt lgkmcnt(2)
	v_mfma_f32_16x16x32_bf16 v[100:103], v[176:179], v[208:211], v[100:103]
	ds_read_b128 v[192:195], v199 offset:49152
	v_mfma_f32_16x16x32_bf16 v[92:95], v[180:183], v[208:211], v[92:95]
	v_mfma_f32_16x16x32_bf16 v[88:91], v[184:187], v[208:211], v[88:91]
	v_mfma_f32_16x16x32_bf16 v[108:111], v[188:191], v[208:211], v[108:111]
	s_waitcnt lgkmcnt(2)
	v_mfma_f32_16x16x32_bf16 v[104:107], v[176:179], v[212:215], v[104:107]
	ds_read_b128 v[208:211], v199 offset:51200
	buffer_load_dwordx4 v[28:31], v197, s[24:27], s39 offen
	s_waitcnt vmcnt(12)
	v_cvt_pk_bf16_f32 v19, v18, v19
	v_cvt_pk_bf16_f32 v18, v16, v17
	v_mfma_f32_16x16x32_bf16 v[96:99], v[180:183], v[212:215], v[96:99]
	ds_write_b64 v198, v[18:19] offset:17408
	v_mfma_f32_16x16x32_bf16 v[84:87], v[184:187], v[212:215], v[84:87]
	v_mfma_f32_16x16x32_bf16 v[80:83], v[188:191], v[212:215], v[80:83]
	s_add_i32 s43, s9, 0xfffe0000
	s_waitcnt lgkmcnt(2)
	v_mfma_f32_16x16x32_bf16 v[72:75], v[176:179], v[192:195], v[72:75]
	ds_read_b128 v[212:215], v199 offset:53248
	v_mfma_f32_16x16x32_bf16 v[64:67], v[180:183], v[192:195], v[64:67]
	v_mfma_f32_16x16x32_bf16 v[60:63], v[184:187], v[192:195], v[60:63]
	v_mfma_f32_16x16x32_bf16 v[76:79], v[188:191], v[192:195], v[76:79]
	s_waitcnt lgkmcnt(2)
	v_mfma_f32_16x16x32_bf16 v[68:71], v[176:179], v[208:211], v[68:71]
	ds_read_b128 v[192:195], v199 offset:37888
	buffer_load_dwordx4 v[16:19], v197, s[24:27], s43 offen
	s_waitcnt vmcnt(12)
	v_cvt_pk_bf16_f32 v27, v26, v27
	v_cvt_pk_bf16_f32 v26, v24, v25
	v_mfma_f32_16x16x32_bf16 v[56:59], v[180:183], v[208:211], v[56:59]
	ds_write_b64 v198, v[26:27] offset:26112
	v_mfma_f32_16x16x32_bf16 v[52:55], v[184:187], v[208:211], v[52:55]
	v_mfma_f32_16x16x32_bf16 v[48:51], v[188:191], v[208:211], v[48:51]
	s_waitcnt lgkmcnt(2)
	v_mfma_f32_16x16x32_bf16 v[44:47], v[176:179], v[212:215], v[44:47]
	ds_read_b128 v[176:179], v199 offset:39936
	v_mfma_f32_16x16x32_bf16 v[40:43], v[180:183], v[212:215], v[40:43]
	ds_read_b64_tr_b16 v[244:245], v205 offset:52224
	ds_read_b64_tr_b16 v[248:249], v205 offset:52256
	ds_read_b64_tr_b16 v[216:217], v205 offset:52288
	ds_read_b64_tr_b16 v[220:221], v205 offset:52320
	ds_read_b64_tr_b16 v[246:247], v206 offset:52224
	ds_read_b64_tr_b16 v[250:251], v206 offset:52256
	ds_read_b64_tr_b16 v[218:219], v206 offset:52288
	ds_read_b64_tr_b16 v[222:223], v206 offset:52320
	v_mfma_f32_16x16x32_bf16 v[36:39], v[184:187], v[212:215], v[36:39]
	v_mfma_f32_16x16x32_bf16 v[32:35], v[188:191], v[212:215], v[32:35]
	s_waitcnt lgkmcnt(3)
	v_mfma_f32_16x16x32_bf16 v[172:175], v[244:247], v[192:195], v[172:175]
	ds_read_b128 v[184:187], v199 offset:41984
	buffer_load_dwordx4 v[24:27], v197, s[24:27], s9 offen
	s_waitcnt vmcnt(12)
	v_cvt_pk_bf16_f32 v15, v14, v15
	v_cvt_pk_bf16_f32 v14, v12, v13
	s_waitcnt lgkmcnt(3)
	v_mfma_f32_16x16x32_bf16 v[168:171], v[248:251], v[192:195], v[168:171]
	ds_write_b64 v198, v[14:15] offset:256
	s_waitcnt lgkmcnt(3)
	v_mfma_f32_16x16x32_bf16 v[164:167], v[216:219], v[192:195], v[164:167]
	s_waitcnt lgkmcnt(2)
	v_mfma_f32_16x16x32_bf16 v[160:163], v[220:223], v[192:195], v[160:163]
	v_mfma_f32_16x16x32_bf16 v[156:159], v[244:247], v[176:179], v[156:159]
	ds_read_b128 v[188:191], v199 offset:44032
	v_mfma_f32_16x16x32_bf16 v[152:155], v[248:251], v[176:179], v[152:155]
	v_mfma_f32_16x16x32_bf16 v[148:151], v[216:219], v[176:179], v[148:151]
	v_mfma_f32_16x16x32_bf16 v[144:147], v[220:223], v[176:179], v[144:147]
	s_waitcnt lgkmcnt(2)
	v_mfma_f32_16x16x32_bf16 v[132:135], v[244:247], v[184:187], v[132:135]
	ds_read_b128 v[176:179], v199 offset:46080
	buffer_load_dwordx4 v[12:15], v197, s[16:19], s38 offen
	s_waitcnt vmcnt(12)
	v_cvt_pk_bf16_f32 v7, v6, v7
	v_cvt_pk_bf16_f32 v6, v4, v5
	v_mfma_f32_16x16x32_bf16 v[124:127], v[248:251], v[184:187], v[124:127]
	ds_write_b64 v198, v[6:7] offset:8960
	v_mfma_f32_16x16x32_bf16 v[120:123], v[216:219], v[184:187], v[120:123]
	v_mfma_f32_16x16x32_bf16 v[140:143], v[220:223], v[184:187], v[140:143]
	s_waitcnt lgkmcnt(2)
	v_mfma_f32_16x16x32_bf16 v[136:139], v[244:247], v[188:191], v[136:139]
	ds_read_b128 v[184:187], v199 offset:48128
	v_mfma_f32_16x16x32_bf16 v[128:131], v[248:251], v[188:191], v[128:131]
	v_mfma_f32_16x16x32_bf16 v[116:119], v[216:219], v[188:191], v[116:119]
	v_mfma_f32_16x16x32_bf16 v[112:115], v[220:223], v[188:191], v[112:115]
	s_waitcnt lgkmcnt(2)
	v_mfma_f32_16x16x32_bf16 v[100:103], v[244:247], v[176:179], v[100:103]
	ds_read_b128 v[188:191], v199 offset:50176
	buffer_load_dwordx4 v[4:7], v197, s[16:19], s39 offen
	s_waitcnt vmcnt(12)
	v_cvt_pk_bf16_f32 v3, v2, v3
	v_cvt_pk_bf16_f32 v2, v0, v1
	v_mfma_f32_16x16x32_bf16 v[92:95], v[248:251], v[176:179], v[92:95]
	ds_write_b64 v198, v[2:3] offset:17664
	v_mfma_f32_16x16x32_bf16 v[88:91], v[216:219], v[176:179], v[88:91]
	v_mfma_f32_16x16x32_bf16 v[108:111], v[220:223], v[176:179], v[108:111]
	s_waitcnt lgkmcnt(2)
	v_mfma_f32_16x16x32_bf16 v[104:107], v[244:247], v[184:187], v[104:107]
	ds_read_b128 v[176:179], v199 offset:52224
	v_mfma_f32_16x16x32_bf16 v[96:99], v[248:251], v[184:187], v[96:99]
	v_mfma_f32_16x16x32_bf16 v[84:87], v[216:219], v[184:187], v[84:87]
	v_mfma_f32_16x16x32_bf16 v[80:83], v[220:223], v[184:187], v[80:83]
	s_waitcnt lgkmcnt(2)
	v_mfma_f32_16x16x32_bf16 v[72:75], v[244:247], v[188:191], v[72:75]
	ds_read_b128 v[252:255], v199 offset:54272
	buffer_load_dwordx4 v[0:3], v197, s[16:19], s43 offen
	s_waitcnt vmcnt(12)
	v_cvt_pk_bf16_f32 v11, v10, v11
	v_cvt_pk_bf16_f32 v10, v8, v9
	v_mfma_f32_16x16x32_bf16 v[64:67], v[248:251], v[188:191], v[64:67]
	ds_write_b64 v198, v[10:11] offset:26368
	v_mfma_f32_16x16x32_bf16 v[60:63], v[216:219], v[188:191], v[60:63]
	v_mfma_f32_16x16x32_bf16 v[76:79], v[220:223], v[188:191], v[76:79]
	s_waitcnt lgkmcnt(2)
	v_mfma_f32_16x16x32_bf16 v[68:71], v[244:247], v[176:179], v[68:71]
	v_mfma_f32_16x16x32_bf16 v[56:59], v[248:251], v[176:179], v[56:59]
	v_mfma_f32_16x16x32_bf16 v[52:55], v[216:219], v[176:179], v[52:55]
	v_mfma_f32_16x16x32_bf16 v[48:51], v[220:223], v[176:179], v[48:51]
	s_waitcnt lgkmcnt(1)
	buffer_load_dwordx4 v[8:11], v197, s[16:19], s9 offen
	s_waitcnt vmcnt(8)
	s_waitcnt lgkmcnt(0)
	s_barrier
	s_add_i32 s8, s8, 2
	s_add_i32 s9, s9, 0x100000
	s_addk_i32 s36, 0x100
	s_cmp_ge_i32 s8, s84
	s_cbranch_scc1 .Lflush_P6
